# MoE combine tail-row blocks: third K-quarter load issued together with the first two (one wait chain per block instead of two)
# speedup vs baseline: 1.0090x; 1.0090x over previous
; __device__ __forceinline__ u32x4 pack8(f32x4 v0, f32x4 v1) { u32x4 w; w.x = cvt_pk_bf16(v0[0], v0[1]); w.y = cvt_pk_bf16(v0[2], v0[3]); w.z = cvt_pk_bf16(v1[0], v1[1]); w.w = cvt_pk_bf16(v1[2], v1[3]); return w; }
; __device__ __forceinline__ void unpack8(u32x4 w, f32x4& v0, f32x4& v1) { v0 = (f32x4){bf_lo(w.x), bf_hi(w.x), bf_lo(w.y), bf_hi(w.y)}; v1 = (f32x4){bf_lo(w.z), bf_hi(w.z), bf_lo(w.w), bf_hi(w.w)}; }
; __global__ void __launch_bounds__(NWAVES * 64, 2) mk_fwd(Args a) {
;     ...
;             { for (int tok = gw; tok < NT; tok += ngw) { const int d0 = tokdest[tok * 2], d1 = tokdest[tok * 2 + 1]; float sq = 0.f;
; #pragma unroll
;                   for (int j = 0; j < 4; ++j) { const size_t o = (size_t)tok * DM + (lane + 64 * j) * 8; f32x4 x0, x1, p0, p1, q0, q1; epi::unpack8(*(const u32x4*)(XR + o), x0, x1);
;                       epi::unpack8(*(const u32x4*)(YB + (size_t)d0 * DM + (lane + 64 * j) * 8), p0, p1); epi::unpack8(*(const u32x4*)(YB + (size_t)d1 * DM + (lane + 64 * j) * 8), q0, q1);
;                       x0 += p0 + q0; x1 += p1 + q1;
; #pragma unroll
;                       for (int dd = 0; dd < 2; ++dd) { const int d = dd ? d1 : d0; if (d >= 16384) {
; #pragma unroll
;                           for (int s = 0; s < 3; ++s) { epi::unpack8(*(const u32x4*)((const bf16_t*)(ws + wsm::YBX) + ((size_t)s * 2048 + (d - 16384)) * DM + (lane + 64 * j) * 8), p0, p1); x0 += p0; x1 += p1; } } } *(u32x4*)(XR + o) = epi::pack8(x0, x1);
.LBB0_2412:
	s_ashr_i32 s19, s18, 31
	s_lshl_b64 s[4:5], s[18:19], 2
	s_add_u32 s4, s8, s4
	s_addc_u32 s5, s9, s5
	global_load_dwordx2 v[34:35], v3, s[4:5]
	s_waitcnt lgkmcnt(0)
	v_lshl_add_u64 v[24:25], s[52:53], 0, v[22:23]
	v_add_co_u32_e32 v36, vcc, s40, v24
	s_nop 1
	v_addc_co_u32_e32 v37, vcc, 0, v25, vcc
	global_load_dwordx4 v[26:29], v[36:37], off
	s_waitcnt vmcnt(1)
	v_readfirstlane_b32 s36, v34
	s_ashr_i32 s37, s36, 31
	v_ashrrev_i32_e32 v41, 31, v35
	v_mov_b32_e32 v40, v35
	s_lshl_b64 s[4:5], s[36:37], 12
	v_lshlrev_b64 v[40:41], 12, v[40:41]
	v_lshl_add_u64 v[38:39], v[14:15], 0, s[4:5]
	v_lshl_add_u64 v[40:41], v[14:15], 0, v[40:41]
	global_load_dwordx4 v[30:33], v[38:39], off
	global_load_dwordx4 v[42:45], v[40:41], off
	global_load_dwordx4 v[132:135], v[36:37], off offset:1024
	global_load_dwordx4 v[136:139], v[38:39], off offset:1024
	global_load_dwordx4 v[140:143], v[40:41], off offset:1024
	global_load_dwordx4 v[144:147], v[36:37], off offset:2048
	global_load_dwordx4 v[148:151], v[38:39], off offset:2048
	global_load_dwordx4 v[152:155], v[40:41], off offset:2048
	global_load_dwordx4 v[156:159], v[36:37], off offset:3072
	global_load_dwordx4 v[160:163], v[38:39], off offset:3072
	global_load_dwordx4 v[164:167], v[40:41], off offset:3072
	s_waitcnt vmcnt(2)
	v_lshlrev_b32_e32 v46, 16, v28
	v_and_b32_e32 v47, 0xffff0000, v28
	v_lshlrev_b32_e32 v48, 16, v29
	v_and_b32_e32 v49, 0xffff0000, v29
	v_readfirstlane_b32 s19, v35
	v_lshlrev_b32_e32 v34, 16, v26
	v_and_b32_e32 v35, 0xffff0000, v26
	v_lshlrev_b32_e32 v26, 16, v27
	v_and_b32_e32 v27, 0xffff0000, v27
	s_cmpk_gt_i32 s36, 0x3fff
	s_cselect_b64 s[6:7], -1, 0
	s_cmpk_lt_i32 s36, 0x4000
	s_waitcnt vmcnt(1)
	v_lshlrev_b32_e32 v28, 16, v30
	v_and_b32_e32 v29, 0xffff0000, v30
	v_lshlrev_b32_e32 v30, 16, v31
	v_and_b32_e32 v31, 0xffff0000, v31
	v_lshlrev_b32_e32 v50, 16, v32
	v_and_b32_e32 v51, 0xffff0000, v32
	v_lshlrev_b32_e32 v32, 16, v33
	v_and_b32_e32 v33, 0xffff0000, v33
	s_waitcnt vmcnt(0)
	v_lshlrev_b32_e32 v52, 16, v42
	v_and_b32_e32 v53, 0xffff0000, v42
	v_lshlrev_b32_e32 v42, 16, v43
	v_and_b32_e32 v43, 0xffff0000, v43
	v_lshlrev_b32_e32 v54, 16, v44
	v_and_b32_e32 v55, 0xffff0000, v44
	v_lshlrev_b32_e32 v44, 16, v45
	v_and_b32_e32 v45, 0xffff0000, v45
	v_pk_add_f32 v[28:29], v[28:29], v[52:53]
	v_pk_add_f32 v[30:31], v[30:31], v[42:43]
	v_pk_add_f32 v[42:43], v[50:51], v[54:55]
	v_pk_add_f32 v[32:33], v[32:33], v[44:45]
	v_pk_add_f32 v[26:27], v[30:31], v[26:27]
	v_pk_add_f32 v[28:29], v[28:29], v[34:35]
	v_pk_add_f32 v[30:31], v[32:33], v[48:49]
	v_pk_add_f32 v[32:33], v[42:43], v[46:47]
	s_cbranch_scc1 .LBB0_2414
	s_add_i32 s12, s36, 0xffffc000
	s_lshl_b64 s[4:5], s[12:13], 12
	v_lshl_add_u64 v[34:35], v[4:5], 0, s[4:5]
	v_add_co_u32_e32 v46, vcc, s41, v34
	global_load_dwordx4 v[42:45], v[34:35], off
	s_nop 0
	v_addc_co_u32_e32 v47, vcc, 0, v35, vcc
	global_load_dwordx4 v[46:49], v[46:47], off
	v_add_co_u32_e32 v34, vcc, s44, v34
	s_nop 1
	v_addc_co_u32_e32 v35, vcc, 0, v35, vcc
	global_load_dwordx4 v[50:53], v[34:35], off
	s_waitcnt vmcnt(2)
	v_lshlrev_b32_e32 v54, 16, v44
	v_lshlrev_b32_e32 v34, 16, v42
	v_and_b32_e32 v35, 0xffff0000, v42
	v_lshlrev_b32_e32 v42, 16, v43
	v_and_b32_e32 v43, 0xffff0000, v43
	v_and_b32_e32 v55, 0xffff0000, v44
	v_lshlrev_b32_e32 v44, 16, v45
	v_and_b32_e32 v45, 0xffff0000, v45
	v_pk_add_f32 v[26:27], v[26:27], v[42:43]
	v_pk_add_f32 v[28:29], v[28:29], v[34:35]
	v_pk_add_f32 v[30:31], v[30:31], v[44:45]
	v_pk_add_f32 v[32:33], v[32:33], v[54:55]
	s_waitcnt vmcnt(1)
	v_lshlrev_b32_e32 v34, 16, v46
	v_and_b32_e32 v35, 0xffff0000, v46
	v_lshlrev_b32_e32 v42, 16, v47
	v_and_b32_e32 v43, 0xffff0000, v47
	v_lshlrev_b32_e32 v44, 16, v48
	v_and_b32_e32 v45, 0xffff0000, v48
	v_lshlrev_b32_e32 v46, 16, v49
	v_and_b32_e32 v47, 0xffff0000, v49
	v_pk_add_f32 v[28:29], v[28:29], v[34:35]
	v_pk_add_f32 v[26:27], v[26:27], v[42:43]
	v_pk_add_f32 v[32:33], v[32:33], v[44:45]
	v_pk_add_f32 v[30:31], v[30:31], v[46:47]
	s_waitcnt vmcnt(0)
	v_lshlrev_b32_e32 v48, 16, v50
	v_and_b32_e32 v49, 0xffff0000, v50
	v_lshlrev_b32_e32 v50, 16, v51
	v_and_b32_e32 v51, 0xffff0000, v51
	v_lshlrev_b32_e32 v54, 16, v52
	v_and_b32_e32 v55, 0xffff0000, v52
	v_lshlrev_b32_e32 v52, 16, v53
	v_and_b32_e32 v53, 0xffff0000, v53
	v_pk_add_f32 v[26:27], v[26:27], v[50:51]
	v_pk_add_f32 v[28:29], v[28:29], v[48:49]
	v_pk_add_f32 v[30:31], v[30:31], v[52:53]
	v_pk_add_f32 v[32:33], v[32:33], v[54:55]
.LBB0_2414:
	s_cmpk_gt_i32 s19, 0x3fff
	s_cselect_b64 s[38:39], -1, 0
	s_cmpk_lt_i32 s19, 0x4000
	s_cbranch_scc1 .LBB0_2416
	s_add_i32 s12, s19, 0xffffc000
	s_lshl_b64 s[4:5], s[12:13], 12
	v_lshl_add_u64 v[34:35], v[4:5], 0, s[4:5]
	v_add_co_u32_e32 v46, vcc, s41, v34
	global_load_dwordx4 v[42:45], v[34:35], off
	s_nop 0
	v_addc_co_u32_e32 v47, vcc, 0, v35, vcc
	global_load_dwordx4 v[46:49], v[46:47], off
	v_add_co_u32_e32 v34, vcc, s44, v34
	s_nop 1
	v_addc_co_u32_e32 v35, vcc, 0, v35, vcc
	global_load_dwordx4 v[50:53], v[34:35], off
	s_waitcnt vmcnt(2)
	v_lshlrev_b32_e32 v54, 16, v44
	v_lshlrev_b32_e32 v34, 16, v42
	v_and_b32_e32 v35, 0xffff0000, v42
	v_lshlrev_b32_e32 v42, 16, v43
	v_and_b32_e32 v43, 0xffff0000, v43
	v_and_b32_e32 v55, 0xffff0000, v44
	v_lshlrev_b32_e32 v44, 16, v45
	v_and_b32_e32 v45, 0xffff0000, v45
	v_pk_add_f32 v[26:27], v[26:27], v[42:43]
	v_pk_add_f32 v[28:29], v[28:29], v[34:35]
	v_pk_add_f32 v[30:31], v[30:31], v[44:45]
	v_pk_add_f32 v[32:33], v[32:33], v[54:55]
	s_waitcnt vmcnt(1)
	v_lshlrev_b32_e32 v34, 16, v46
	v_and_b32_e32 v35, 0xffff0000, v46
	v_lshlrev_b32_e32 v42, 16, v47
	v_and_b32_e32 v43, 0xffff0000, v47
	v_lshlrev_b32_e32 v44, 16, v48
	v_and_b32_e32 v45, 0xffff0000, v48
	v_lshlrev_b32_e32 v46, 16, v49
	v_and_b32_e32 v47, 0xffff0000, v49
	v_pk_add_f32 v[28:29], v[28:29], v[34:35]
	v_pk_add_f32 v[26:27], v[26:27], v[42:43]
	v_pk_add_f32 v[32:33], v[32:33], v[44:45]
	v_pk_add_f32 v[30:31], v[30:31], v[46:47]
	s_waitcnt vmcnt(0)
	v_lshlrev_b32_e32 v48, 16, v50
	v_and_b32_e32 v49, 0xffff0000, v50
	v_lshlrev_b32_e32 v50, 16, v51
	v_and_b32_e32 v51, 0xffff0000, v51
	v_lshlrev_b32_e32 v54, 16, v52
	v_and_b32_e32 v55, 0xffff0000, v52
	v_lshlrev_b32_e32 v52, 16, v53
	v_and_b32_e32 v53, 0xffff0000, v53
	v_pk_add_f32 v[26:27], v[26:27], v[50:51]
	v_pk_add_f32 v[28:29], v[28:29], v[48:49]
	v_pk_add_f32 v[30:31], v[30:31], v[52:53]
	v_pk_add_f32 v[32:33], v[32:33], v[54:55]
; __device__ __forceinline__ unsigned pk4_fp8(float a, float b, float c, float d) { int w = 0; w = __builtin_amdgcn_cvt_pk_fp8_f32(a, b, w, false); w = __builtin_amdgcn_cvt_pk_fp8_f32(c, d, w, true); return (unsigned)w; }
; __device__ __forceinline__ u32x4 pack8(f32x4 v0, f32x4 v1) { u32x4 w; w.x = cvt_pk_bf16(v0[0], v0[1]); w.y = cvt_pk_bf16(v0[2], v0[3]); w.z = cvt_pk_bf16(v1[0], v1[1]); w.w = cvt_pk_bf16(v1[2], v1[3]); return w; }
; __device__ __forceinline__ void unpack8(u32x4 w, f32x4& v0, f32x4& v1) { v0 = (f32x4){bf_lo(w.x), bf_hi(w.x), bf_lo(w.y), bf_hi(w.y)}; v1 = (f32x4){bf_lo(w.z), bf_hi(w.z), bf_lo(w.w), bf_hi(w.w)}; }
; __global__ void __launch_bounds__(NWAVES * 64, 2) mk_fwd(Args a) {
;     ...
;                   for (int j = 0; j < 4; ++j) { const size_t o = (size_t)tok * DM + (lane + 64 * j) * 8; f32x4 x0, x1, p0, p1, q0, q1; epi::unpack8(*(const u32x4*)(XR + o), x0, x1);
;                       epi::unpack8(*(const u32x4*)(YB + (size_t)d0 * DM + (lane + 64 * j) * 8), p0, p1); epi::unpack8(*(const u32x4*)(YB + (size_t)d1 * DM + (lane + 64 * j) * 8), q0, q1);
;                       x0 += p0 + q0; x1 += p1 + q1;
; #pragma unroll
;                       for (int dd = 0; dd < 2; ++dd) { const int d = dd ? d1 : d0; if (d >= 16384) {
; #pragma unroll
;                           for (int s = 0; s < 3; ++s) { epi::unpack8(*(const u32x4*)((const bf16_t*)(ws + wsm::YBX) + ((size_t)s * 2048 + (d - 16384)) * DM + (lane + 64 * j) * 8), p0, p1); x0 += p0; x1 += p1; } } } *(u32x4*)(XR + o) = epi::pack8(x0, x1);
;                       const float* gp = a.in[28] + DM + (lane + 64 * j) * 8; const f32x4 y0 = x0 * *(const f32x4*)gp, y1 = x1 * *(const f32x4*)(gp + 4);
;                       if constexpr (F8P) *(u32x2*)((unsigned char*)x2b + o) = (u32x2){pk4_fp8(y0[0], y0[1], y0[2], y0[3]), pk4_fp8(y1[0], y1[1], y1[2], y1[3])}; else *(u32x4*)(x2b + o) = epi::pack8(y0, y1);
.LBB0_2416:
	v_lshl_add_u64 v[34:35], v[24:25], 0, s[20:21]
	v_cvt_pk_bf16_f32 v42, v28, v29
	v_cvt_pk_bf16_f32 v43, v26, v27
	v_cvt_pk_bf16_f32 v44, v32, v33
	v_cvt_pk_bf16_f32 v45, v30, v31
	global_store_dwordx4 v[34:35], v[42:45], off
	s_nop 1
	v_mov_b32_e32 v42, v100
	v_mov_b32_e32 v43, v101
	v_mov_b32_e32 v44, v102
	v_mov_b32_e32 v45, v103
	s_nop 0
	s_nop 1
	v_mov_b32_e32 v46, v104
	v_mov_b32_e32 v47, v105
	v_mov_b32_e32 v48, v106
	v_mov_b32_e32 v49, v107
	v_cndmask_b32_e64 v2, 0, 1, s[6:7]
	v_cmp_ne_u32_e64 s[4:5], 1, v2
	s_nop 0
	v_pk_mul_f32 v[34:35], v[26:27], v[44:45]
	v_pk_mul_f32 v[42:43], v[28:29], v[42:43]
	s_nop 0
	v_pk_mul_f32 v[44:45], v[32:33], v[46:47]
	v_cvt_pk_bf16_f32 v42, v42, v43
	v_cvt_pk_bf16_f32 v43, v34, v35
	v_add_co_u32_e32 v34, vcc, s45, v24
	v_pk_mul_f32 v[48:49], v[30:31], v[48:49]
	s_nop 0
	v_addc_co_u32_e32 v35, vcc, 0, v25, vcc
	v_cvt_pk_bf16_f32 v44, v44, v45
	v_cvt_pk_bf16_f32 v45, v48, v49
	global_store_dwordx4 v[34:35], v[42:45], off
	s_nop 1
	v_mov_b32_e32 v46, v132
	v_mov_b32_e32 v47, v133
	v_mov_b32_e32 v48, v134
	v_mov_b32_e32 v49, v135
	s_nop 0
	s_nop 1
	v_mov_b32_e32 v42, v136
	v_mov_b32_e32 v43, v137
	v_mov_b32_e32 v44, v138
	v_mov_b32_e32 v45, v139
	s_nop 1
	v_mov_b32_e32 v50, v140
	v_mov_b32_e32 v51, v141
	v_mov_b32_e32 v52, v142
	v_mov_b32_e32 v53, v143
	s_andn2_b64 vcc, exec, s[6:7]
	s_nop 0
	v_lshlrev_b32_e32 v54, 16, v46
	s_nop 0
	v_lshlrev_b32_e32 v58, 16, v42
	v_and_b32_e32 v59, 0xffff0000, v42
	v_lshlrev_b32_e32 v42, 16, v43
	v_and_b32_e32 v43, 0xffff0000, v43
	v_lshlrev_b32_e32 v60, 16, v44
	v_and_b32_e32 v61, 0xffff0000, v44
	v_lshlrev_b32_e32 v44, 16, v45
	v_and_b32_e32 v45, 0xffff0000, v45
	s_nop 0
	v_lshlrev_b32_e32 v62, 16, v50
	v_and_b32_e32 v63, 0xffff0000, v50
	v_lshlrev_b32_e32 v50, 16, v51
	v_and_b32_e32 v51, 0xffff0000, v51
	v_lshlrev_b32_e32 v64, 16, v52
	v_and_b32_e32 v65, 0xffff0000, v52
	v_lshlrev_b32_e32 v52, 16, v53
	v_and_b32_e32 v53, 0xffff0000, v53
	v_and_b32_e32 v55, 0xffff0000, v46
	v_lshlrev_b32_e32 v46, 16, v47
	v_and_b32_e32 v47, 0xffff0000, v47
	v_lshlrev_b32_e32 v56, 16, v48
	v_and_b32_e32 v57, 0xffff0000, v48
	v_lshlrev_b32_e32 v48, 16, v49
	v_and_b32_e32 v49, 0xffff0000, v49
	v_pk_add_f32 v[58:59], v[58:59], v[62:63]
	v_pk_add_f32 v[42:43], v[42:43], v[50:51]
	v_pk_add_f32 v[50:51], v[60:61], v[64:65]
	v_pk_add_f32 v[52:53], v[44:45], v[52:53]
	v_pk_add_f32 v[42:43], v[42:43], v[46:47]
	v_pk_add_f32 v[44:45], v[58:59], v[54:55]
	v_pk_add_f32 v[46:47], v[52:53], v[48:49]
	v_pk_add_f32 v[48:49], v[50:51], v[56:57]
	s_cbranch_vccnz .LBB0_2418
	s_add_i32 s12, s36, 0xffffc000
	s_lshl_b64 s[6:7], s[12:13], 12
	v_lshl_add_u64 v[58:59], v[16:17], 0, s[6:7]
	v_add_co_u32_e32 v54, vcc, s41, v58
	global_load_dwordx4 v[50:53], v[58:59], off
	s_nop 0
	v_addc_co_u32_e32 v55, vcc, 0, v59, vcc
	global_load_dwordx4 v[54:57], v[54:55], off
	v_add_co_u32_e32 v58, vcc, s44, v58
	s_nop 1
	v_addc_co_u32_e32 v59, vcc, 0, v59, vcc
	global_load_dwordx4 v[58:61], v[58:59], off
	s_waitcnt vmcnt(2)
	v_lshlrev_b32_e32 v62, 16, v50
	v_and_b32_e32 v63, 0xffff0000, v50
	v_lshlrev_b32_e32 v50, 16, v51
	v_and_b32_e32 v51, 0xffff0000, v51
	v_lshlrev_b32_e32 v64, 16, v52
	v_and_b32_e32 v65, 0xffff0000, v52
	v_lshlrev_b32_e32 v52, 16, v53
	v_and_b32_e32 v53, 0xffff0000, v53
	v_pk_add_f32 v[42:43], v[42:43], v[50:51]
	v_pk_add_f32 v[44:45], v[44:45], v[62:63]
	v_pk_add_f32 v[46:47], v[46:47], v[52:53]
	v_pk_add_f32 v[48:49], v[48:49], v[64:65]
	s_waitcnt vmcnt(1)
	v_lshlrev_b32_e32 v50, 16, v54
	v_and_b32_e32 v51, 0xffff0000, v54
	v_lshlrev_b32_e32 v52, 16, v55
	v_and_b32_e32 v53, 0xffff0000, v55
	v_lshlrev_b32_e32 v54, 16, v56
	v_and_b32_e32 v55, 0xffff0000, v56
	v_lshlrev_b32_e32 v56, 16, v57
	v_and_b32_e32 v57, 0xffff0000, v57
	v_pk_add_f32 v[44:45], v[44:45], v[50:51]
	v_pk_add_f32 v[42:43], v[42:43], v[52:53]
	v_pk_add_f32 v[48:49], v[48:49], v[54:55]
	v_pk_add_f32 v[46:47], v[46:47], v[56:57]
	s_waitcnt vmcnt(0)
	v_lshlrev_b32_e32 v62, 16, v58
	v_and_b32_e32 v63, 0xffff0000, v58
	v_lshlrev_b32_e32 v58, 16, v59
	v_and_b32_e32 v59, 0xffff0000, v59
	v_lshlrev_b32_e32 v64, 16, v60
	v_and_b32_e32 v65, 0xffff0000, v60
	v_lshlrev_b32_e32 v60, 16, v61
	v_and_b32_e32 v61, 0xffff0000, v61
	v_pk_add_f32 v[42:43], v[42:43], v[58:59]
	v_pk_add_f32 v[44:45], v[44:45], v[62:63]
	v_pk_add_f32 v[46:47], v[46:47], v[60:61]
	v_pk_add_f32 v[48:49], v[48:49], v[64:65]
.LBB0_2418:
	v_cndmask_b32_e64 v2, 0, 1, s[38:39]
	v_cmp_ne_u32_e64 s[6:7], 1, v2
	s_andn2_b64 vcc, exec, s[38:39]
	s_cbranch_vccnz .LBB0_2420
	s_add_i32 s12, s19, 0xffffc000
	s_lshl_b64 s[38:39], s[12:13], 12
	v_lshl_add_u64 v[58:59], v[16:17], 0, s[38:39]
	v_add_co_u32_e32 v54, vcc, s41, v58
	global_load_dwordx4 v[50:53], v[58:59], off
	s_nop 0
	v_addc_co_u32_e32 v55, vcc, 0, v59, vcc
	global_load_dwordx4 v[54:57], v[54:55], off
	v_add_co_u32_e32 v58, vcc, s44, v58
	s_nop 1
	v_addc_co_u32_e32 v59, vcc, 0, v59, vcc
	global_load_dwordx4 v[58:61], v[58:59], off
	s_waitcnt vmcnt(2)
	v_lshlrev_b32_e32 v62, 16, v50
	v_and_b32_e32 v63, 0xffff0000, v50
	v_lshlrev_b32_e32 v50, 16, v51
	v_and_b32_e32 v51, 0xffff0000, v51
	v_lshlrev_b32_e32 v64, 16, v52
	v_and_b32_e32 v65, 0xffff0000, v52
	v_lshlrev_b32_e32 v52, 16, v53
	v_and_b32_e32 v53, 0xffff0000, v53
	v_pk_add_f32 v[42:43], v[42:43], v[50:51]
	v_pk_add_f32 v[44:45], v[44:45], v[62:63]
	v_pk_add_f32 v[46:47], v[46:47], v[52:53]
	v_pk_add_f32 v[48:49], v[48:49], v[64:65]
	s_waitcnt vmcnt(1)
	v_lshlrev_b32_e32 v50, 16, v54
	v_and_b32_e32 v51, 0xffff0000, v54
	v_lshlrev_b32_e32 v52, 16, v55
	v_and_b32_e32 v53, 0xffff0000, v55
	v_lshlrev_b32_e32 v54, 16, v56
	v_and_b32_e32 v55, 0xffff0000, v56
	v_lshlrev_b32_e32 v56, 16, v57
	v_and_b32_e32 v57, 0xffff0000, v57
	v_pk_add_f32 v[44:45], v[44:45], v[50:51]
	v_pk_add_f32 v[42:43], v[42:43], v[52:53]
	v_pk_add_f32 v[48:49], v[48:49], v[54:55]
	v_pk_add_f32 v[46:47], v[46:47], v[56:57]
	s_waitcnt vmcnt(0)
	v_lshlrev_b32_e32 v62, 16, v58
	v_and_b32_e32 v63, 0xffff0000, v58
	v_lshlrev_b32_e32 v58, 16, v59
	v_and_b32_e32 v59, 0xffff0000, v59
	v_lshlrev_b32_e32 v64, 16, v60
	v_and_b32_e32 v65, 0xffff0000, v60
	v_lshlrev_b32_e32 v60, 16, v61
	v_and_b32_e32 v61, 0xffff0000, v61
	v_pk_add_f32 v[42:43], v[42:43], v[58:59]
	v_pk_add_f32 v[44:45], v[44:45], v[62:63]
	v_pk_add_f32 v[46:47], v[46:47], v[60:61]
	v_pk_add_f32 v[48:49], v[48:49], v[64:65]
; __device__ __forceinline__ unsigned pk4_fp8(float a, float b, float c, float d) { int w = 0; w = __builtin_amdgcn_cvt_pk_fp8_f32(a, b, w, false); w = __builtin_amdgcn_cvt_pk_fp8_f32(c, d, w, true); return (unsigned)w; }
; __device__ __forceinline__ u32x4 pack8(f32x4 v0, f32x4 v1) { u32x4 w; w.x = cvt_pk_bf16(v0[0], v0[1]); w.y = cvt_pk_bf16(v0[2], v0[3]); w.z = cvt_pk_bf16(v1[0], v1[1]); w.w = cvt_pk_bf16(v1[2], v1[3]); return w; }
; __device__ __forceinline__ void unpack8(u32x4 w, f32x4& v0, f32x4& v1) { v0 = (f32x4){bf_lo(w.x), bf_hi(w.x), bf_lo(w.y), bf_hi(w.y)}; v1 = (f32x4){bf_lo(w.z), bf_hi(w.z), bf_lo(w.w), bf_hi(w.w)}; }
; __global__ void __launch_bounds__(NWAVES * 64, 2) mk_fwd(Args a) {
;     ...
;                   for (int j = 0; j < 4; ++j) { const size_t o = (size_t)tok * DM + (lane + 64 * j) * 8; f32x4 x0, x1, p0, p1, q0, q1; epi::unpack8(*(const u32x4*)(XR + o), x0, x1);
;                       epi::unpack8(*(const u32x4*)(YB + (size_t)d0 * DM + (lane + 64 * j) * 8), p0, p1); epi::unpack8(*(const u32x4*)(YB + (size_t)d1 * DM + (lane + 64 * j) * 8), q0, q1);
;                       x0 += p0 + q0; x1 += p1 + q1;
; #pragma unroll
;                       for (int dd = 0; dd < 2; ++dd) { const int d = dd ? d1 : d0; if (d >= 16384) {
; #pragma unroll
;                           for (int s = 0; s < 3; ++s) { epi::unpack8(*(const u32x4*)((const bf16_t*)(ws + wsm::YBX) + ((size_t)s * 2048 + (d - 16384)) * DM + (lane + 64 * j) * 8), p0, p1); x0 += p0; x1 += p1; } } } *(u32x4*)(XR + o) = epi::pack8(x0, x1);
;                       const float* gp = a.in[28] + DM + (lane + 64 * j) * 8; const f32x4 y0 = x0 * *(const f32x4*)gp, y1 = x1 * *(const f32x4*)(gp + 4);
;                       if constexpr (F8P) *(u32x2*)((unsigned char*)x2b + o) = (u32x2){pk4_fp8(y0[0], y0[1], y0[2], y0[3]), pk4_fp8(y1[0], y1[1], y1[2], y1[3])}; else *(u32x4*)(x2b + o) = epi::pack8(y0, y1);
.LBB0_2420:
	v_lshl_add_u64 v[54:55], v[24:25], 0, s[22:23]
	v_cvt_pk_bf16_f32 v50, v44, v45
	v_cvt_pk_bf16_f32 v51, v42, v43
	v_cvt_pk_bf16_f32 v52, v48, v49
	v_cvt_pk_bf16_f32 v53, v46, v47
	global_store_dwordx4 v[54:55], v[50:53], off
	s_nop 1
	v_mov_b32_e32 v50, v108
	v_mov_b32_e32 v51, v109
	v_mov_b32_e32 v52, v110
	v_mov_b32_e32 v53, v111
	s_nop 0
	s_nop 1
	v_mov_b32_e32 v54, v112
	v_mov_b32_e32 v55, v113
	v_mov_b32_e32 v56, v114
	v_mov_b32_e32 v57, v115
	s_and_b64 vcc, exec, s[4:5]
	s_nop 0
	v_pk_mul_f32 v[52:53], v[42:43], v[52:53]
	v_pk_mul_f32 v[50:51], v[44:45], v[50:51]
	s_nop 0
	v_pk_mul_f32 v[56:57], v[46:47], v[56:57]
	v_pk_mul_f32 v[54:55], v[48:49], v[54:55]
	v_cvt_pk_bf16_f32 v50, v50, v51
	v_cvt_pk_bf16_f32 v51, v52, v53
	s_nop 0
	v_cvt_pk_bf16_f32 v52, v54, v55
	v_cvt_pk_bf16_f32 v53, v56, v57
	global_store_dwordx4 v[34:35], v[50:53], off offset:1024
	s_nop 1
	v_mov_b32_e32 v54, v144
	v_mov_b32_e32 v55, v145
	v_mov_b32_e32 v56, v146
	v_mov_b32_e32 v57, v147
	s_nop 0
	s_nop 1
	v_mov_b32_e32 v50, v148
	v_mov_b32_e32 v51, v149
	v_mov_b32_e32 v52, v150
	v_mov_b32_e32 v53, v151
	s_nop 1
	v_mov_b32_e32 v58, v152
	v_mov_b32_e32 v59, v153
	v_mov_b32_e32 v60, v154
	v_mov_b32_e32 v61, v155
	s_nop 0
	v_lshlrev_b32_e32 v66, 16, v50
	v_and_b32_e32 v67, 0xffff0000, v50
	v_lshlrev_b32_e32 v50, 16, v51
	v_and_b32_e32 v51, 0xffff0000, v51
	v_lshlrev_b32_e32 v68, 16, v52
	v_and_b32_e32 v69, 0xffff0000, v52
	v_lshlrev_b32_e32 v52, 16, v53
	v_and_b32_e32 v53, 0xffff0000, v53
	s_nop 0
	v_lshlrev_b32_e32 v70, 16, v58
	v_and_b32_e32 v71, 0xffff0000, v58
	v_lshlrev_b32_e32 v58, 16, v59
	v_and_b32_e32 v59, 0xffff0000, v59
	v_lshlrev_b32_e32 v72, 16, v60
	v_and_b32_e32 v73, 0xffff0000, v60
	v_lshlrev_b32_e32 v60, 16, v61
	v_and_b32_e32 v61, 0xffff0000, v61
	v_lshlrev_b32_e32 v62, 16, v54
	v_and_b32_e32 v63, 0xffff0000, v54
	v_lshlrev_b32_e32 v54, 16, v55
	v_and_b32_e32 v55, 0xffff0000, v55
	v_lshlrev_b32_e32 v64, 16, v56
	v_and_b32_e32 v65, 0xffff0000, v56
	v_lshlrev_b32_e32 v56, 16, v57
	v_and_b32_e32 v57, 0xffff0000, v57
	v_pk_add_f32 v[66:67], v[66:67], v[70:71]
	v_pk_add_f32 v[50:51], v[50:51], v[58:59]
	v_pk_add_f32 v[58:59], v[68:69], v[72:73]
	v_pk_add_f32 v[60:61], v[52:53], v[60:61]
	v_pk_add_f32 v[50:51], v[50:51], v[54:55]
	v_pk_add_f32 v[52:53], v[66:67], v[62:63]
	v_pk_add_f32 v[54:55], v[60:61], v[56:57]
	v_pk_add_f32 v[56:57], v[58:59], v[64:65]
	s_cbranch_vccnz .LBB0_2422
	s_add_i32 s12, s36, 0xffffc000
	s_lshl_b64 s[38:39], s[12:13], 12
	v_lshl_add_u64 v[66:67], v[18:19], 0, s[38:39]
	v_add_co_u32_e32 v62, vcc, s41, v66
	global_load_dwordx4 v[58:61], v[66:67], off
	s_nop 0
	v_addc_co_u32_e32 v63, vcc, 0, v67, vcc
	global_load_dwordx4 v[62:65], v[62:63], off
	v_add_co_u32_e32 v66, vcc, s44, v66
	s_nop 1
	v_addc_co_u32_e32 v67, vcc, 0, v67, vcc
	global_load_dwordx4 v[66:69], v[66:67], off
	s_waitcnt vmcnt(2)
	v_lshlrev_b32_e32 v70, 16, v58
	v_and_b32_e32 v71, 0xffff0000, v58
	v_lshlrev_b32_e32 v58, 16, v59
	v_and_b32_e32 v59, 0xffff0000, v59
	v_lshlrev_b32_e32 v72, 16, v60
	v_and_b32_e32 v73, 0xffff0000, v60
	v_lshlrev_b32_e32 v60, 16, v61
	v_and_b32_e32 v61, 0xffff0000, v61
	v_pk_add_f32 v[50:51], v[50:51], v[58:59]
	v_pk_add_f32 v[52:53], v[52:53], v[70:71]
	v_pk_add_f32 v[54:55], v[54:55], v[60:61]
	v_pk_add_f32 v[56:57], v[56:57], v[72:73]
	s_waitcnt vmcnt(1)
	v_lshlrev_b32_e32 v58, 16, v62
	v_and_b32_e32 v59, 0xffff0000, v62
	v_lshlrev_b32_e32 v60, 16, v63
	v_and_b32_e32 v61, 0xffff0000, v63
	v_lshlrev_b32_e32 v62, 16, v64
	v_and_b32_e32 v63, 0xffff0000, v64
	v_lshlrev_b32_e32 v64, 16, v65
	v_and_b32_e32 v65, 0xffff0000, v65
	v_pk_add_f32 v[52:53], v[52:53], v[58:59]
	v_pk_add_f32 v[50:51], v[50:51], v[60:61]
	v_pk_add_f32 v[56:57], v[56:57], v[62:63]
	v_pk_add_f32 v[54:55], v[54:55], v[64:65]
	s_waitcnt vmcnt(0)
	v_lshlrev_b32_e32 v70, 16, v66
	v_and_b32_e32 v71, 0xffff0000, v66
	v_lshlrev_b32_e32 v66, 16, v67
	v_and_b32_e32 v67, 0xffff0000, v67
	v_lshlrev_b32_e32 v72, 16, v68
	v_and_b32_e32 v73, 0xffff0000, v68
	v_lshlrev_b32_e32 v68, 16, v69
	v_and_b32_e32 v69, 0xffff0000, v69
	v_pk_add_f32 v[50:51], v[50:51], v[66:67]
	v_pk_add_f32 v[52:53], v[52:53], v[70:71]
	v_pk_add_f32 v[54:55], v[54:55], v[68:69]
	v_pk_add_f32 v[56:57], v[56:57], v[72:73]
.LBB0_2422:
	s_and_b64 vcc, exec, s[6:7]
	s_cbranch_vccnz .LBB0_2424
	s_add_i32 s12, s19, 0xffffc000
	s_lshl_b64 s[38:39], s[12:13], 12
	v_lshl_add_u64 v[66:67], v[18:19], 0, s[38:39]
	v_add_co_u32_e32 v62, vcc, s41, v66
	global_load_dwordx4 v[58:61], v[66:67], off
	s_nop 0
	v_addc_co_u32_e32 v63, vcc, 0, v67, vcc
	global_load_dwordx4 v[62:65], v[62:63], off
	v_add_co_u32_e32 v66, vcc, s44, v66
	s_nop 1
	v_addc_co_u32_e32 v67, vcc, 0, v67, vcc
	global_load_dwordx4 v[66:69], v[66:67], off
	s_waitcnt vmcnt(2)
	v_lshlrev_b32_e32 v70, 16, v58
	v_and_b32_e32 v71, 0xffff0000, v58
	v_lshlrev_b32_e32 v58, 16, v59
	v_and_b32_e32 v59, 0xffff0000, v59
	v_lshlrev_b32_e32 v72, 16, v60
	v_and_b32_e32 v73, 0xffff0000, v60
	v_lshlrev_b32_e32 v60, 16, v61
	v_and_b32_e32 v61, 0xffff0000, v61
	v_pk_add_f32 v[50:51], v[50:51], v[58:59]
	v_pk_add_f32 v[52:53], v[52:53], v[70:71]
	v_pk_add_f32 v[54:55], v[54:55], v[60:61]
	v_pk_add_f32 v[56:57], v[56:57], v[72:73]
	s_waitcnt vmcnt(1)
	v_lshlrev_b32_e32 v58, 16, v62
	v_and_b32_e32 v59, 0xffff0000, v62
	v_lshlrev_b32_e32 v60, 16, v63
	v_and_b32_e32 v61, 0xffff0000, v63
	v_lshlrev_b32_e32 v62, 16, v64
	v_and_b32_e32 v63, 0xffff0000, v64
	v_lshlrev_b32_e32 v64, 16, v65
	v_and_b32_e32 v65, 0xffff0000, v65
	v_pk_add_f32 v[52:53], v[52:53], v[58:59]
	v_pk_add_f32 v[50:51], v[50:51], v[60:61]
	v_pk_add_f32 v[56:57], v[56:57], v[62:63]
	v_pk_add_f32 v[54:55], v[54:55], v[64:65]
	s_waitcnt vmcnt(0)
	v_lshlrev_b32_e32 v70, 16, v66
	v_and_b32_e32 v71, 0xffff0000, v66
	v_lshlrev_b32_e32 v66, 16, v67
	v_and_b32_e32 v67, 0xffff0000, v67
	v_lshlrev_b32_e32 v72, 16, v68
	v_and_b32_e32 v73, 0xffff0000, v68
	v_lshlrev_b32_e32 v68, 16, v69
	v_and_b32_e32 v69, 0xffff0000, v69
	v_pk_add_f32 v[50:51], v[50:51], v[66:67]
	v_pk_add_f32 v[52:53], v[52:53], v[70:71]
	v_pk_add_f32 v[54:55], v[54:55], v[68:69]
	v_pk_add_f32 v[56:57], v[56:57], v[72:73]
; __device__ __forceinline__ unsigned pk4_fp8(float a, float b, float c, float d) { int w = 0; w = __builtin_amdgcn_cvt_pk_fp8_f32(a, b, w, false); w = __builtin_amdgcn_cvt_pk_fp8_f32(c, d, w, true); return (unsigned)w; }
; __device__ __forceinline__ u32x4 pack8(f32x4 v0, f32x4 v1) { u32x4 w; w.x = cvt_pk_bf16(v0[0], v0[1]); w.y = cvt_pk_bf16(v0[2], v0[3]); w.z = cvt_pk_bf16(v1[0], v1[1]); w.w = cvt_pk_bf16(v1[2], v1[3]); return w; }
; __device__ __forceinline__ void unpack8(u32x4 w, f32x4& v0, f32x4& v1) { v0 = (f32x4){bf_lo(w.x), bf_hi(w.x), bf_lo(w.y), bf_hi(w.y)}; v1 = (f32x4){bf_lo(w.z), bf_hi(w.z), bf_lo(w.w), bf_hi(w.w)}; }
; __global__ void __launch_bounds__(NWAVES * 64, 2) mk_fwd(Args a) {
;     ...
;                   for (int j = 0; j < 4; ++j) { const size_t o = (size_t)tok * DM + (lane + 64 * j) * 8; f32x4 x0, x1, p0, p1, q0, q1; epi::unpack8(*(const u32x4*)(XR + o), x0, x1);
;                       epi::unpack8(*(const u32x4*)(YB + (size_t)d0 * DM + (lane + 64 * j) * 8), p0, p1); epi::unpack8(*(const u32x4*)(YB + (size_t)d1 * DM + (lane + 64 * j) * 8), q0, q1);
;                       x0 += p0 + q0; x1 += p1 + q1;
; #pragma unroll
;                       for (int dd = 0; dd < 2; ++dd) { const int d = dd ? d1 : d0; if (d >= 16384) {
; #pragma unroll
;                           for (int s = 0; s < 3; ++s) { epi::unpack8(*(const u32x4*)((const bf16_t*)(ws + wsm::YBX) + ((size_t)s * 2048 + (d - 16384)) * DM + (lane + 64 * j) * 8), p0, p1); x0 += p0; x1 += p1; } } } *(u32x4*)(XR + o) = epi::pack8(x0, x1);
;                       const float* gp = a.in[28] + DM + (lane + 64 * j) * 8; const f32x4 y0 = x0 * *(const f32x4*)gp, y1 = x1 * *(const f32x4*)(gp + 4);
;                       if constexpr (F8P) *(u32x2*)((unsigned char*)x2b + o) = (u32x2){pk4_fp8(y0[0], y0[1], y0[2], y0[3]), pk4_fp8(y1[0], y1[1], y1[2], y1[3])}; else *(u32x4*)(x2b + o) = epi::pack8(y0, y1);
.LBB0_2424:
	v_lshl_add_u64 v[62:63], v[24:25], 0, s[24:25]
	v_cvt_pk_bf16_f32 v58, v52, v53
	v_cvt_pk_bf16_f32 v59, v50, v51
	v_cvt_pk_bf16_f32 v60, v56, v57
	v_cvt_pk_bf16_f32 v61, v54, v55
	global_store_dwordx4 v[62:63], v[58:61], off
	s_nop 1
	v_mov_b32_e32 v58, v116
	v_mov_b32_e32 v59, v117
	v_mov_b32_e32 v60, v118
	v_mov_b32_e32 v61, v119
	s_nop 0
	s_nop 1
	v_mov_b32_e32 v62, v120
	v_mov_b32_e32 v63, v121
	v_mov_b32_e32 v64, v122
	v_mov_b32_e32 v65, v123
	s_and_b64 vcc, exec, s[4:5]
	s_nop 0
	v_pk_mul_f32 v[60:61], v[50:51], v[60:61]
	v_pk_mul_f32 v[58:59], v[52:53], v[58:59]
	s_nop 0
	v_pk_mul_f32 v[64:65], v[54:55], v[64:65]
	v_pk_mul_f32 v[62:63], v[56:57], v[62:63]
	v_cvt_pk_bf16_f32 v58, v58, v59
	v_cvt_pk_bf16_f32 v59, v60, v61
	s_nop 0
	v_cvt_pk_bf16_f32 v60, v62, v63
	v_cvt_pk_bf16_f32 v61, v64, v65
	global_store_dwordx4 v[34:35], v[58:61], off offset:2048
	s_nop 1
	v_mov_b32_e32 v62, v156
	v_mov_b32_e32 v63, v157
	v_mov_b32_e32 v64, v158
	v_mov_b32_e32 v65, v159
	s_nop 0
	s_nop 1
	v_mov_b32_e32 v36, v160
	v_mov_b32_e32 v37, v161
	v_mov_b32_e32 v38, v162
	v_mov_b32_e32 v39, v163
	s_nop 0
	s_nop 1
	v_mov_b32_e32 v58, v164
	v_mov_b32_e32 v59, v165
	v_mov_b32_e32 v60, v166
	v_mov_b32_e32 v61, v167
	s_nop 0
	v_lshlrev_b32_e32 v68, 16, v36
	v_and_b32_e32 v69, 0xffff0000, v36
	v_lshlrev_b32_e32 v36, 16, v37
	v_and_b32_e32 v37, 0xffff0000, v37
	v_lshlrev_b32_e32 v70, 16, v38
	v_and_b32_e32 v71, 0xffff0000, v38
	v_lshlrev_b32_e32 v38, 16, v39
	v_and_b32_e32 v39, 0xffff0000, v39
	s_nop 0
	v_lshlrev_b32_e32 v72, 16, v58
	v_and_b32_e32 v73, 0xffff0000, v58
	v_lshlrev_b32_e32 v58, 16, v59
	v_and_b32_e32 v59, 0xffff0000, v59
	v_lshlrev_b32_e32 v74, 16, v60
	v_and_b32_e32 v75, 0xffff0000, v60
	v_lshlrev_b32_e32 v60, 16, v61
	v_and_b32_e32 v61, 0xffff0000, v61
	v_lshlrev_b32_e32 v40, 16, v62
	v_and_b32_e32 v41, 0xffff0000, v62
	v_lshlrev_b32_e32 v62, 16, v63
	v_and_b32_e32 v63, 0xffff0000, v63
	v_lshlrev_b32_e32 v66, 16, v64
	v_and_b32_e32 v67, 0xffff0000, v64
	v_lshlrev_b32_e32 v64, 16, v65
	v_and_b32_e32 v65, 0xffff0000, v65
	v_pk_add_f32 v[68:69], v[68:69], v[72:73]
	v_pk_add_f32 v[36:37], v[36:37], v[58:59]
	v_pk_add_f32 v[58:59], v[70:71], v[74:75]
	v_pk_add_f32 v[60:61], v[38:39], v[60:61]
	v_pk_add_f32 v[38:39], v[36:37], v[62:63]
	v_pk_add_f32 v[36:37], v[68:69], v[40:41]
	v_pk_add_f32 v[40:41], v[60:61], v[64:65]
	v_pk_add_f32 v[58:59], v[58:59], v[66:67]
	s_cbranch_vccnz .LBB0_2426
	s_add_i32 s12, s36, 0xffffc000
	s_lshl_b64 s[4:5], s[12:13], 12
	v_lshl_add_u64 v[68:69], v[20:21], 0, s[4:5]
	v_add_co_u32_e32 v64, vcc, s41, v68
	global_load_dwordx4 v[60:63], v[68:69], off
	s_nop 0
	v_addc_co_u32_e32 v65, vcc, 0, v69, vcc
	global_load_dwordx4 v[64:67], v[64:65], off
	v_add_co_u32_e32 v68, vcc, s44, v68
	s_nop 1
	v_addc_co_u32_e32 v69, vcc, 0, v69, vcc
	global_load_dwordx4 v[68:71], v[68:69], off
	s_waitcnt vmcnt(2)
	v_lshlrev_b32_e32 v72, 16, v60
	v_and_b32_e32 v73, 0xffff0000, v60
	v_lshlrev_b32_e32 v60, 16, v61
	v_and_b32_e32 v61, 0xffff0000, v61
	v_lshlrev_b32_e32 v74, 16, v62
	v_and_b32_e32 v75, 0xffff0000, v62
	v_lshlrev_b32_e32 v62, 16, v63
	v_and_b32_e32 v63, 0xffff0000, v63
	v_pk_add_f32 v[38:39], v[38:39], v[60:61]
	v_pk_add_f32 v[36:37], v[36:37], v[72:73]
	v_pk_add_f32 v[40:41], v[40:41], v[62:63]
	v_pk_add_f32 v[58:59], v[58:59], v[74:75]
	s_waitcnt vmcnt(1)
	v_lshlrev_b32_e32 v60, 16, v64
	v_and_b32_e32 v61, 0xffff0000, v64
	v_lshlrev_b32_e32 v62, 16, v65
	v_and_b32_e32 v63, 0xffff0000, v65
	v_lshlrev_b32_e32 v64, 16, v66
	v_and_b32_e32 v65, 0xffff0000, v66
	v_lshlrev_b32_e32 v66, 16, v67
	v_and_b32_e32 v67, 0xffff0000, v67
	v_pk_add_f32 v[36:37], v[36:37], v[60:61]
	v_pk_add_f32 v[38:39], v[38:39], v[62:63]
	v_pk_add_f32 v[58:59], v[58:59], v[64:65]
	v_pk_add_f32 v[40:41], v[40:41], v[66:67]
	s_waitcnt vmcnt(0)
	v_lshlrev_b32_e32 v72, 16, v68
	v_and_b32_e32 v73, 0xffff0000, v68
	v_lshlrev_b32_e32 v68, 16, v69
	v_and_b32_e32 v69, 0xffff0000, v69
	v_lshlrev_b32_e32 v74, 16, v70
	v_and_b32_e32 v75, 0xffff0000, v70
	v_lshlrev_b32_e32 v70, 16, v71
	v_and_b32_e32 v71, 0xffff0000, v71
	v_pk_add_f32 v[38:39], v[38:39], v[68:69]
	v_pk_add_f32 v[36:37], v[36:37], v[72:73]
	v_pk_add_f32 v[40:41], v[40:41], v[70:71]
	v_pk_add_f32 v[58:59], v[58:59], v[74:75]
.LBB0_2426:
	s_and_b64 vcc, exec, s[6:7]
	s_cbranch_vccnz .LBB0_2428
	s_add_i32 s12, s19, 0xffffc000
	s_lshl_b64 s[4:5], s[12:13], 12
	v_lshl_add_u64 v[68:69], v[20:21], 0, s[4:5]
	v_add_co_u32_e32 v64, vcc, s41, v68
	global_load_dwordx4 v[60:63], v[68:69], off
	s_nop 0
	v_addc_co_u32_e32 v65, vcc, 0, v69, vcc
	global_load_dwordx4 v[64:67], v[64:65], off
	v_add_co_u32_e32 v68, vcc, s44, v68
	s_nop 1
	v_addc_co_u32_e32 v69, vcc, 0, v69, vcc
	global_load_dwordx4 v[68:71], v[68:69], off
	s_waitcnt vmcnt(2)
	v_lshlrev_b32_e32 v72, 16, v60
	v_and_b32_e32 v73, 0xffff0000, v60
	v_lshlrev_b32_e32 v60, 16, v61
	v_and_b32_e32 v61, 0xffff0000, v61
	v_lshlrev_b32_e32 v74, 16, v62
	v_and_b32_e32 v75, 0xffff0000, v62
	v_lshlrev_b32_e32 v62, 16, v63
	v_and_b32_e32 v63, 0xffff0000, v63
	v_pk_add_f32 v[38:39], v[38:39], v[60:61]
	v_pk_add_f32 v[36:37], v[36:37], v[72:73]
	v_pk_add_f32 v[40:41], v[40:41], v[62:63]
	v_pk_add_f32 v[58:59], v[58:59], v[74:75]
	s_waitcnt vmcnt(1)
	v_lshlrev_b32_e32 v60, 16, v64
	v_and_b32_e32 v61, 0xffff0000, v64
	v_lshlrev_b32_e32 v62, 16, v65
	v_and_b32_e32 v63, 0xffff0000, v65
	v_lshlrev_b32_e32 v64, 16, v66
	v_and_b32_e32 v65, 0xffff0000, v66
	v_lshlrev_b32_e32 v66, 16, v67
	v_and_b32_e32 v67, 0xffff0000, v67
	v_pk_add_f32 v[36:37], v[36:37], v[60:61]
	v_pk_add_f32 v[38:39], v[38:39], v[62:63]
	v_pk_add_f32 v[58:59], v[58:59], v[64:65]
	v_pk_add_f32 v[40:41], v[40:41], v[66:67]
	s_waitcnt vmcnt(0)
	v_lshlrev_b32_e32 v72, 16, v68
	v_and_b32_e32 v73, 0xffff0000, v68
	v_lshlrev_b32_e32 v68, 16, v69
	v_and_b32_e32 v69, 0xffff0000, v69
	v_lshlrev_b32_e32 v74, 16, v70
	v_and_b32_e32 v75, 0xffff0000, v70
	v_lshlrev_b32_e32 v70, 16, v71
	v_and_b32_e32 v71, 0xffff0000, v71
	v_pk_add_f32 v[38:39], v[38:39], v[68:69]
	v_pk_add_f32 v[36:37], v[36:37], v[72:73]
	v_pk_add_f32 v[40:41], v[40:41], v[70:71]
	v_pk_add_f32 v[58:59], v[58:59], v[74:75]
